# diff-attn fixed softmax reference two log2 units above the first-tile maximum (more fp8 headroom, fewer redone units)
# baseline (speedup 1.0000x reference)
.LBB0_1211:
	s_and_b32 s37, s95, 0xffffffc0
	v_lshlrev_b32_e32 v6, 2, v5
	v_lshlrev_b32_e32 v3, 6, v4
	v_and_b32_e32 v6, 48, v6
	s_cmp_lg_u32 0, -1
	v_bitop3_b32 v194, v6, v3, v2 bitop3:0xde
	s_cselect_b32 s38, 0, 0
	v_lshlrev_b32_e32 v2, 3, v5
	v_and_b32_e32 v193, 63, v5
	v_add_u32_e32 v183, s38, v194
	s_addk_i32 s38, 0x4000
	v_and_b32_e32 v2, 32, v2
	s_lshl_b32 s37, s37, 2
	v_add_u32_e32 v188, s38, v194
	v_sub_u32_e32 v195, 16, v2
	v_lshrrev_b32_e32 v2, 5, v193
	s_add_i32 s78, s37, 0
	v_add_u32_e32 v190, v183, v195
	s_mov_b64 s[38:39], -1
	s_and_b64 vcc, exec, s[6:7]
	v_add_u32_e32 v189, v188, v195
	v_cmp_gt_u32_e64 s[6:7], 32, v193
	v_lshlrev_b32_e32 v186, 4, v2
	v_lshl_add_u32 v187, v4, 2, s78
	v_and_b32_e32 v248, 31, v193
	v_mov_b32_e32 v249, 0x38383838
	v_cmp_eq_u32_e64 s[100:101], 0, v248
	v_lshrrev_b32_e32 v250, 4, v193
	s_nop 0
	v_cndmask_b32_e64 v146, 0, v249, s[100:101]
	v_cmp_eq_u32_e64 s[100:101], 17, v248
	v_and_b32_e32 v248, 15, v193
	v_lshlrev_b32_e32 v248, 6, v248
	v_cndmask_b32_e64 v146, v146, v249, s[100:101]
	v_lshl_add_u32 v250, v250, 4, v248
	v_add_u32_e32 v250, s78, v250
	v_mov_b32_e32 v147, v146
	v_mov_b32_e32 v148, v146
	v_mov_b32_e32 v149, v146
	v_mov_b32_e32 v150, v146
	v_mov_b32_e32 v151, v146
	v_mov_b32_e32 v152, v146
	v_mov_b32_e32 v153, v146
	s_cbranch_vccz .LBB0_1264
	ds_read_b128 v[18:21], v183 offset:0
	ds_read_b128 v[22:25], v190 offset:0
	ds_read_b128 v[34:37], v183 offset:0x800
	ds_read_b128 v[38:41], v190 offset:0x800
	s_waitcnt lgkmcnt(0)
	s_waitcnt vmcnt(0)
	v_mfma_f32_32x32x64_f8f6f4 v[18:33], v[18:25], v[154:161], 0
	s_mov_b32 s37, s36
	s_mov_b32 s38, s36
	s_mov_b32 s39, s36
	s_mov_b32 s40, s36
	s_mov_b32 s41, s36
	s_mov_b32 s42, s36
	s_mov_b32 s43, s36
	s_mov_b32 s44, s36
	s_mov_b32 s45, s36
	s_mov_b32 s46, s36
	s_mov_b32 s47, s36
	s_mov_b32 s48, s36
	s_mov_b32 s49, s36
	s_mov_b32 s50, s36
	s_mov_b32 s51, s36
	v_mov_b64_e32 v[2:3], s[36:37]
	v_mov_b64_e32 v[4:5], s[38:39]
	v_mov_b64_e32 v[6:7], s[40:41]
	v_mov_b64_e32 v[8:9], s[42:43]
	v_mov_b64_e32 v[10:11], s[44:45]
	v_mov_b64_e32 v[12:13], s[46:47]
	v_mov_b64_e32 v[14:15], s[48:49]
	v_mov_b64_e32 v[16:17], s[50:51]
	v_max_f32_e32 v42, v19, v19
	v_max_f32_e32 v43, v18, v18
	v_max_f32_e32 v42, v43, v42
	v_max3_f32 v42, v42, v20, v21
	v_max3_f32 v42, v42, v22, v23
	v_max3_f32 v42, v42, v24, v25
	v_max3_f32 v42, v42, v26, v27
	v_max3_f32 v42, v42, v28, v29
	v_max3_f32 v50, v42, v30, v31
	v_mfma_f32_32x32x64_f8f6f4 v[34:49], v[34:41], v[154:161], 0
	v_max3_f32 v50, v50, v32, v33
	s_cmp_lg_u32 0, -1
	s_cselect_b32 s37, 0, 0
	v_mov_b32_e32 v130, v181
	v_mov_b32_e32 v131, v181
	s_add_i32 s38, s37, 0x1000
	s_waitcnt vmcnt(0) lgkmcnt(0)
	s_barrier
	v_add_u32_e32 v207, s38, v194
	v_add_u32_e32 v209, v207, v195
	s_nop 11
	v_max3_f32 v50, v50, v34, v35
	v_max3_f32 v50, v50, v36, v37
	v_max3_f32 v50, v50, v38, v39
	v_max3_f32 v50, v50, v40, v41
	v_max3_f32 v50, v50, v42, v43
	v_max3_f32 v50, v50, v44, v45
	v_max3_f32 v50, v50, v46, v47
	v_max3_f32 v50, v50, v48, v49
	v_mov_b32_e32 v51, v50
	s_nop 1
	v_permlane32_swap_b32_e32 v50, v51
	v_max_f32_e32 v51, v51, v51
	v_max_f32_e32 v50, v50, v50
	v_max_f32_e32 v50, v50, v51
	s_cmp_eq_u32 s98, 0
	s_cselect_b32 s100, 0x40000000, 0xc0600000
	v_add_f32_e32 v198, s100, v50
	v_sub_f32_e32 v18, v18, v198
	v_sub_f32_e32 v19, v19, v198
	v_sub_f32_e32 v22, v22, v198
	v_sub_f32_e32 v23, v23, v198
	v_exp_f32_e32 v50, v18
	v_exp_f32_e32 v51, v19
	v_exp_f32_e32 v54, v22
	v_exp_f32_e32 v55, v23
	v_xor_b32_e32 v82, 0x80000000, v198
	v_sub_f32_e32 v20, v20, v198
	v_sub_f32_e32 v21, v21, v198
	v_sub_f32_e32 v24, v24, v198
	v_sub_f32_e32 v25, v25, v198
	v_mov_b32_e32 v83, v82
	v_mov_b32_e32 v84, v82
	v_mov_b32_e32 v85, v82
	v_mov_b32_e32 v86, v82
	v_mov_b32_e32 v87, v82
	v_mov_b32_e32 v88, v82
	v_mov_b32_e32 v89, v82
	v_mov_b32_e32 v90, v82
	v_mov_b32_e32 v91, v82
	v_mov_b32_e32 v92, v82
	v_mov_b32_e32 v93, v82
	v_mov_b32_e32 v94, v82
	v_mov_b32_e32 v95, v82
	v_mov_b32_e32 v96, v82
	v_mov_b32_e32 v97, v82
	v_exp_f32_e32 v52, v20
	v_exp_f32_e32 v53, v21
	v_exp_f32_e32 v56, v24
	v_exp_f32_e32 v57, v25
	v_cvt_pk_fp8_f32 v130, v50, v51
	v_cvt_pk_fp8_f32 v131, v54, v55
	ds_read_b128 v[18:21], v207 offset:0
	v_sub_f32_e32 v26, v26, v198
	v_sub_f32_e32 v27, v27, v198
	v_sub_f32_e32 v28, v28, v198
	v_sub_f32_e32 v29, v29, v198
	ds_read_b128 v[22:25], v209 offset:0
	v_sub_f32_e32 v34, v34, v198
	v_sub_f32_e32 v35, v35, v198
	v_sub_f32_e32 v36, v36, v198
	v_sub_f32_e32 v37, v37, v198
	v_sub_f32_e32 v38, v38, v198
	v_sub_f32_e32 v39, v39, v198
	v_sub_f32_e32 v40, v40, v198
	v_sub_f32_e32 v41, v41, v198
	v_sub_f32_e32 v42, v42, v198
	v_sub_f32_e32 v43, v43, v198
	v_sub_f32_e32 v44, v44, v198
	v_sub_f32_e32 v45, v45, v198
	v_sub_f32_e32 v30, v30, v198
	v_sub_f32_e32 v46, v46, v198
	v_sub_f32_e32 v31, v31, v198
	v_sub_f32_e32 v47, v47, v198
	v_sub_f32_e32 v32, v32, v198
	v_sub_f32_e32 v48, v48, v198
	v_sub_f32_e32 v33, v33, v198
	v_sub_f32_e32 v49, v49, v198
	v_exp_f32_e32 v58, v26
	v_exp_f32_e32 v59, v27
	v_exp_f32_e32 v60, v28
	v_exp_f32_e32 v61, v29
	ds_read_b128 v[26:29], v207 offset:0x800
	v_exp_f32_e32 v34, v34
	v_exp_f32_e32 v35, v35
	v_exp_f32_e32 v36, v36
	v_exp_f32_e32 v37, v37
	v_exp_f32_e32 v38, v38
	v_exp_f32_e32 v39, v39
	v_exp_f32_e32 v40, v40
	v_exp_f32_e32 v41, v41
	v_exp_f32_e32 v42, v42
	v_exp_f32_e32 v43, v43
	v_exp_f32_e32 v44, v44
	v_exp_f32_e32 v45, v45
	v_exp_f32_e32 v62, v30
	v_exp_f32_e32 v46, v46
	v_exp_f32_e32 v63, v31
	v_exp_f32_e32 v47, v47
	v_exp_f32_e32 v64, v32
	v_exp_f32_e32 v48, v48
	v_exp_f32_e32 v65, v33
	v_exp_f32_e32 v49, v49
	ds_read_b128 v[30:33], v209 offset:0x800
	v_cvt_pk_fp8_f32 v130, v52, v53 op_sel:[0,0,1]
	v_cvt_pk_fp8_f32 v131, v56, v57 op_sel:[0,0,1]
	s_waitcnt lgkmcnt(2)
	v_mfma_f32_32x32x64_f8f6f4 v[98:113], v[18:25], v[154:161], v[82:97]
	v_mov_b32_e32 v132, v181
	v_mov_b32_e32 v133, v181
	v_cvt_pk_fp8_f32 v132, v58, v59
	v_cvt_pk_fp8_f32 v133, v62, v63
	ds_read_b128 v[170:173], v188 offset:0
	ds_read_b128 v[174:177], v189 offset:0
	v_cvt_pk_fp8_f32 v132, v60, v61 op_sel:[0,0,1]
	v_cvt_pk_fp8_f32 v133, v64, v65 op_sel:[0,0,1]
	s_waitcnt lgkmcnt(2)
	v_mov_b64_e32 v[128:129], v[96:97]
	v_mov_b64_e32 v[126:127], v[94:95]
	v_mov_b64_e32 v[124:125], v[92:93]
	v_mov_b64_e32 v[122:123], v[90:91]
	v_mov_b64_e32 v[120:121], v[88:89]
	v_mov_b64_e32 v[118:119], v[86:87]
	v_mov_b64_e32 v[116:117], v[84:85]
	v_mov_b64_e32 v[114:115], v[82:83]
	v_mov_b32_e32 v134, v181
	v_mov_b32_e32 v135, v181
	v_mfma_f32_32x32x64_f8f6f4 v[114:129], v[26:33], v[154:161], v[114:129]
	v_mov_b32_e32 v136, v181
	v_mov_b32_e32 v137, v181
	v_cvt_pk_fp8_f32 v134, v34, v35
	v_cvt_pk_fp8_f32 v135, v38, v39
	v_cvt_pk_fp8_f32 v136, v42, v43
	v_cvt_pk_fp8_f32 v137, v46, v47
	v_cvt_pk_fp8_f32 v134, v36, v37 op_sel:[0,0,1]
	v_cvt_pk_fp8_f32 v135, v40, v41 op_sel:[0,0,1]
	v_cvt_pk_fp8_f32 v136, v44, v45 op_sel:[0,0,1]
	v_cvt_pk_fp8_f32 v137, v48, v49 op_sel:[0,0,1]
	s_nop 0
	ds_read_b128 v[138:141], v188 offset:0x800
	ds_read_b128 v[142:145], v189 offset:0x800
	s_nop 0
	v_mfma_f32_16x16x128_f8f6f4 v[18:21], v[130:137], v[146:153], 0
	s_add_i32 s38, s37, 0x2000
	v_add_u32_e32 v205, s38, v194
	s_add_i32 s38, s37, 0x6000
	v_add_u32_e32 v203, s38, v194
	s_add_i32 s38, s37, 0x3000
	s_waitcnt vmcnt(0) lgkmcnt(0)
	s_barrier
	v_add_u32_e32 v201, s38, v194
	s_add_i32 s38, s37, 0x8000
	s_add_i32 s37, s37, 0xa000
	v_add_u32_e32 v199, s38, v194
	v_add_u32_e32 v196, s37, v194
	v_mov_b64_e32 v[48:49], v[16:17]
	v_mov_b64_e32 v[64:65], v[16:17]
	v_mov_b64_e32 v[80:81], v[16:17]
	v_add_u32_e32 v206, v205, v195
	v_add_u32_e32 v204, v203, v195
	v_add_u32_e32 v202, v201, v195
	v_add_u32_e32 v200, v199, v195
	v_add_u32_e32 v197, v196, v195
	s_mov_b32 s37, -2
	v_mov_b64_e32 v[46:47], v[14:15]
	v_mov_b64_e32 v[44:45], v[12:13]
	v_mov_b64_e32 v[42:43], v[10:11]
	v_mov_b64_e32 v[40:41], v[8:9]
	v_mov_b64_e32 v[38:39], v[6:7]
	v_mov_b64_e32 v[36:37], v[4:5]
	v_mov_b64_e32 v[34:35], v[2:3]
	v_mov_b64_e32 v[62:63], v[14:15]
	v_mov_b64_e32 v[60:61], v[12:13]
	v_mov_b64_e32 v[58:59], v[10:11]
	v_mov_b64_e32 v[56:57], v[8:9]
	v_mov_b64_e32 v[54:55], v[6:7]
	v_mov_b64_e32 v[52:53], v[4:5]
	v_mov_b64_e32 v[50:51], v[2:3]
	v_mov_b64_e32 v[78:79], v[14:15]
	v_mov_b64_e32 v[76:77], v[12:13]
	v_mov_b64_e32 v[74:75], v[10:11]
	v_mov_b64_e32 v[72:73], v[8:9]
	v_mov_b64_e32 v[70:71], v[6:7]
	v_mov_b64_e32 v[68:69], v[4:5]
	v_mov_b64_e32 v[66:67], v[2:3]
	s_branch .LBB0_1215

.LBB0_1264:
	s_lshl_b32 s94, s77, 8
	s_add_i32 s77, s94, 0x8000
	s_and_b64 vcc, exec, s[38:39]
	s_cbranch_vccz .LBB0_1317
	ds_read_b128 v[18:21], v183 offset:0
	ds_read_b128 v[22:25], v190 offset:0
	ds_read_b128 v[34:37], v183 offset:0x800
	ds_read_b128 v[38:41], v190 offset:0x800
	s_waitcnt lgkmcnt(0)
	s_waitcnt vmcnt(0)
	s_nop 9
	v_mfma_f32_32x32x64_f8f6f4 v[18:33], v[18:25], v[154:161], 0
	s_mov_b32 s37, s36
	s_mov_b32 s38, s36
	s_mov_b32 s39, s36
	s_mov_b32 s40, s36
	s_mov_b32 s41, s36
	s_mov_b32 s42, s36
	s_mov_b32 s43, s36
	s_mov_b32 s44, s36
	s_mov_b32 s45, s36
	s_mov_b32 s46, s36
	s_mov_b32 s47, s36
	s_mov_b32 s48, s36
	s_mov_b32 s49, s36
	s_mov_b32 s50, s36
	s_mov_b32 s51, s36
	v_mov_b64_e32 v[2:3], s[36:37]
	v_mov_b64_e32 v[4:5], s[38:39]
	v_mov_b64_e32 v[6:7], s[40:41]
	v_mov_b64_e32 v[8:9], s[42:43]
	v_mov_b64_e32 v[10:11], s[44:45]
	v_mov_b64_e32 v[12:13], s[46:47]
	v_mov_b64_e32 v[14:15], s[48:49]
	v_mov_b64_e32 v[16:17], s[50:51]
	v_max_f32_e32 v42, v19, v19
	v_max_f32_e32 v43, v18, v18
	v_max_f32_e32 v42, v43, v42
	v_max3_f32 v42, v42, v20, v21
	v_max3_f32 v42, v42, v22, v23
	v_max3_f32 v42, v42, v24, v25
	v_max3_f32 v42, v42, v26, v27
	v_max3_f32 v42, v42, v28, v29
	v_max3_f32 v50, v42, v30, v31
	v_mfma_f32_32x32x64_f8f6f4 v[34:49], v[34:41], v[154:161], 0
	v_max3_f32 v50, v50, v32, v33
	s_lshl_b32 s45, s81, 10
	s_lshl_b32 s46, s80, 10
	s_cmp_lg_u32 0, -1
	s_cselect_b32 s38, 0, 0
	s_add_i32 s37, s38, 0x2000
	s_add_i32 s39, s38, 0x3000
	s_add_i32 s6, s38, 0x1000
	v_add_u32_e32 v203, s37, v194
	s_add_i32 s37, s38, 0x6000
	v_add_u32_e32 v199, s39, v194
	s_add_i32 s39, s38, 0x8000
	s_add_i32 s38, s38, 0xa000
	v_add_u32_e32 v205, s6, v194
	v_add_u32_e32 v201, s37, v194
	s_nop 4
	v_max3_f32 v50, v50, v34, v35
	v_max3_f32 v50, v50, v36, v37
	v_max3_f32 v50, v50, v38, v39
	v_max3_f32 v50, v50, v40, v41
	v_max3_f32 v50, v50, v42, v43
	v_max3_f32 v50, v50, v44, v45
	v_max3_f32 v50, v50, v46, v47
	v_max3_f32 v50, v50, v48, v49
	v_mov_b32_e32 v51, v50
	s_nop 1
	v_permlane32_swap_b32_e32 v50, v51
	v_max_f32_e32 v51, v51, v51
	v_max_f32_e32 v50, v50, v50
	v_max_f32_e32 v50, v50, v51
	s_cmp_eq_u32 s98, 0
	s_cselect_b32 s100, 0x40000000, 0xc0600000
	v_add_f32_e32 v198, s100, v50
	v_add_u32_e32 v196, s39, v194
	v_add_u32_e32 v194, s38, v194
	s_lshl_b32 s38, s95, 4
	v_sub_f32_e32 v18, v18, v198
	s_and_b32 s38, s38, 0xfffffc00
	s_ashr_i32 s89, s88, 31
	v_exp_f32_e32 v114, v18
	s_or_b32 s40, s88, 0x100
	s_add_i32 s41, s94, 0x4100
	s_or_b32 s42, s88, 0x140
	s_add_i32 s43, s94, 0x4140
	v_lshl_or_b32 v18, v193, 4, s38
	s_lshl_b64 s[38:39], s[88:89], 10
	s_add_u32 s38, s38, s87
	v_xor_b32_e32 v82, 0x80000000, v198
	v_sub_f32_e32 v34, v34, v198
	v_sub_f32_e32 v19, v19, v198
	v_sub_f32_e32 v35, v35, v198
	v_sub_f32_e32 v20, v20, v198
	v_sub_f32_e32 v36, v36, v198
	v_sub_f32_e32 v21, v21, v198
	v_sub_f32_e32 v37, v37, v198
	v_sub_f32_e32 v22, v22, v198
	v_sub_f32_e32 v38, v38, v198
	v_sub_f32_e32 v23, v23, v198
	v_sub_f32_e32 v39, v39, v198
	v_sub_f32_e32 v24, v24, v198
	v_sub_f32_e32 v40, v40, v198
	v_sub_f32_e32 v25, v25, v198
	v_sub_f32_e32 v41, v41, v198
	v_sub_f32_e32 v26, v26, v198
	v_sub_f32_e32 v42, v42, v198
	v_sub_f32_e32 v27, v27, v198
	v_sub_f32_e32 v43, v43, v198
	v_sub_f32_e32 v28, v28, v198
	v_sub_f32_e32 v44, v44, v198
	v_sub_f32_e32 v29, v29, v198
	v_sub_f32_e32 v45, v45, v198
	v_sub_f32_e32 v30, v30, v198
	v_sub_f32_e32 v46, v46, v198
	v_sub_f32_e32 v31, v31, v198
	v_sub_f32_e32 v47, v47, v198
	v_sub_f32_e32 v32, v32, v198
	v_sub_f32_e32 v48, v48, v198
	v_sub_f32_e32 v33, v33, v198
	v_sub_f32_e32 v49, v49, v198
	s_addc_u32 s39, s39, s76
	v_mov_b32_e32 v83, v82
	v_mov_b32_e32 v84, v82
	v_mov_b32_e32 v85, v82
	v_mov_b32_e32 v86, v82
	v_mov_b32_e32 v87, v82
	v_mov_b32_e32 v88, v82
	v_mov_b32_e32 v89, v82
	v_mov_b32_e32 v90, v82
	v_mov_b32_e32 v91, v82
	v_mov_b32_e32 v92, v82
	v_mov_b32_e32 v93, v82
	v_mov_b32_e32 v94, v82
	v_mov_b32_e32 v95, v82
	v_mov_b32_e32 v96, v82
	v_mov_b32_e32 v97, v82
	v_exp_f32_e32 v98, v34
	v_exp_f32_e32 v115, v19
	v_exp_f32_e32 v99, v35
	v_exp_f32_e32 v116, v20
	v_exp_f32_e32 v100, v36
	v_exp_f32_e32 v117, v21
	v_exp_f32_e32 v101, v37
	v_exp_f32_e32 v118, v22
	v_exp_f32_e32 v102, v38
	v_exp_f32_e32 v119, v23
	v_exp_f32_e32 v103, v39
	v_exp_f32_e32 v120, v24
	v_exp_f32_e32 v104, v40
	v_exp_f32_e32 v121, v25
	v_exp_f32_e32 v105, v41
	v_exp_f32_e32 v122, v26
	v_exp_f32_e32 v106, v42
	v_exp_f32_e32 v123, v27
	v_exp_f32_e32 v107, v43
	v_exp_f32_e32 v124, v28
	v_exp_f32_e32 v108, v44
	v_exp_f32_e32 v125, v29
	v_exp_f32_e32 v109, v45
	v_exp_f32_e32 v126, v30
	v_exp_f32_e32 v110, v46
	v_exp_f32_e32 v127, v31
	v_exp_f32_e32 v111, v47
	v_exp_f32_e32 v128, v32
	v_exp_f32_e32 v112, v48
	v_exp_f32_e32 v129, v33
	v_exp_f32_e32 v113, v49
	v_mov_b32_e32 v19, v181
	s_add_u32 s38, s38, 0x29c30000
	s_waitcnt vmcnt(3) lgkmcnt(0)
	s_barrier
	v_lshl_add_u64 v[172:173], s[92:93], 0, v[18:19]
	s_addc_u32 s39, s39, 0
	v_add3_u32 v18, s79, v191, v192
	v_lshl_add_u64 v[174:175], s[38:39], 0, v[18:19]
	v_mov_b32_e32 v162, 0
	v_mov_b64_e32 v[48:49], v[16:17]
	v_mov_b64_e32 v[64:65], v[16:17]
	v_mov_b64_e32 v[80:81], v[16:17]
	v_mov_b64_e32 v[32:33], v[16:17]
	v_lshl_add_u64 v[170:171], s[28:29], 0, v[180:181]
	v_add_u32_e32 v206, v205, v195
	v_cmp_gt_u32_e64 s[6:7], 32, v193
	v_add_u32_e32 v204, v203, v195
	v_add_u32_e32 v202, v201, v195
	s_movk_i32 s37, 0x100
	v_add_u32_e32 v200, v199, v195
	v_add_u32_e32 v197, v196, v195
	v_add_u32_e32 v195, v194, v195
	s_mov_b32 s44, -3
	s_add_i32 s45, s45, 0
	s_add_i32 s46, s46, 0
	v_mov_b64_e32 v[46:47], v[14:15]
	v_mov_b64_e32 v[44:45], v[12:13]
	v_mov_b64_e32 v[42:43], v[10:11]
	v_mov_b64_e32 v[40:41], v[8:9]
	v_mov_b64_e32 v[38:39], v[6:7]
	v_mov_b64_e32 v[36:37], v[4:5]
	v_mov_b64_e32 v[34:35], v[2:3]
	v_mov_b64_e32 v[62:63], v[14:15]
	v_mov_b64_e32 v[60:61], v[12:13]
	v_mov_b64_e32 v[58:59], v[10:11]
	v_mov_b64_e32 v[56:57], v[8:9]
	v_mov_b64_e32 v[54:55], v[6:7]
	v_mov_b64_e32 v[52:53], v[4:5]
	v_mov_b64_e32 v[50:51], v[2:3]
	v_mov_b64_e32 v[78:79], v[14:15]
	v_mov_b64_e32 v[76:77], v[12:13]
	v_mov_b64_e32 v[74:75], v[10:11]
	v_mov_b64_e32 v[72:73], v[8:9]
	v_mov_b64_e32 v[70:71], v[6:7]
	v_mov_b64_e32 v[68:69], v[4:5]
	v_mov_b64_e32 v[66:67], v[2:3]
	v_mov_b64_e32 v[30:31], v[14:15]
	v_mov_b64_e32 v[28:29], v[12:13]
	v_mov_b64_e32 v[26:27], v[10:11]
	v_mov_b64_e32 v[24:25], v[8:9]
	v_mov_b64_e32 v[22:23], v[6:7]
	v_mov_b64_e32 v[20:21], v[4:5]
	v_mov_b64_e32 v[18:19], v[2:3]
	v_mov_b32_e32 v163, v162
	v_mov_b32_e32 v164, v162
	v_mov_b32_e32 v165, v162
	v_mov_b32_e32 v166, v162
	v_mov_b32_e32 v167, v162
	v_mov_b32_e32 v168, v162
	v_mov_b32_e32 v169, v162
	s_branch .LBB0_1268

.LBB0_1323:
	s_and_b32 s37, s80, 0xffffffc0
	v_lshlrev_b32_e32 v6, 2, v5
	v_lshlrev_b32_e32 v3, 6, v4
	v_and_b32_e32 v6, 48, v6
	s_cmp_lg_u32 0, -1
	v_bitop3_b32 v194, v6, v3, v2 bitop3:0xde
	s_cselect_b32 s38, 0, 0
	v_lshlrev_b32_e32 v2, 3, v5
	v_and_b32_e32 v193, 63, v5
	v_add_u32_e32 v183, s38, v194
	s_addk_i32 s38, 0x4000
	v_and_b32_e32 v2, 32, v2
	s_lshl_b32 s37, s37, 2
	v_add_u32_e32 v188, s38, v194
	v_sub_u32_e32 v195, 16, v2
	v_lshrrev_b32_e32 v2, 5, v193
	s_add_i32 s78, s37, 0
	v_add_u32_e32 v190, v183, v195
	s_mov_b64 s[38:39], -1
	s_and_b64 vcc, exec, s[6:7]
	v_add_u32_e32 v189, v188, v195
	v_cmp_gt_u32_e64 s[6:7], 32, v193
	v_lshlrev_b32_e32 v186, 4, v2
	v_lshl_add_u32 v187, v4, 2, s78
	v_and_b32_e32 v248, 31, v193
	v_mov_b32_e32 v249, 0x38383838
	v_cmp_eq_u32_e64 s[100:101], 0, v248
	v_lshrrev_b32_e32 v250, 4, v193
	s_nop 0
	v_cndmask_b32_e64 v146, 0, v249, s[100:101]
	v_cmp_eq_u32_e64 s[100:101], 17, v248
	v_and_b32_e32 v248, 15, v193
	v_lshlrev_b32_e32 v248, 6, v248
	v_cndmask_b32_e64 v146, v146, v249, s[100:101]
	v_lshl_add_u32 v250, v250, 4, v248
	v_add_u32_e32 v250, s78, v250
	v_mov_b32_e32 v147, v146
	v_mov_b32_e32 v148, v146
	v_mov_b32_e32 v149, v146
	v_mov_b32_e32 v150, v146
	v_mov_b32_e32 v151, v146
	v_mov_b32_e32 v152, v146
	v_mov_b32_e32 v153, v146
	s_cbranch_vccz .LBB0_1376
	ds_read_b128 v[18:21], v183 offset:0
	ds_read_b128 v[22:25], v190 offset:0
	ds_read_b128 v[34:37], v183 offset:0x800
	ds_read_b128 v[38:41], v190 offset:0x800
	s_waitcnt lgkmcnt(0)
	s_waitcnt vmcnt(0)
	v_mfma_f32_32x32x64_f8f6f4 v[18:33], v[18:25], v[154:161], 0
	s_mov_b32 s37, s36
	s_mov_b32 s38, s36
	s_mov_b32 s39, s36
	s_mov_b32 s40, s36
	s_mov_b32 s41, s36
	s_mov_b32 s42, s36
	s_mov_b32 s43, s36
	s_mov_b32 s44, s36
	s_mov_b32 s45, s36
	s_mov_b32 s46, s36
	s_mov_b32 s47, s36
	s_mov_b32 s48, s36
	s_mov_b32 s49, s36
	s_mov_b32 s50, s36
	s_mov_b32 s51, s36
	v_mov_b64_e32 v[2:3], s[36:37]
	v_mov_b64_e32 v[4:5], s[38:39]
	v_mov_b64_e32 v[6:7], s[40:41]
	v_mov_b64_e32 v[8:9], s[42:43]
	v_mov_b64_e32 v[10:11], s[44:45]
	v_mov_b64_e32 v[12:13], s[46:47]
	v_mov_b64_e32 v[14:15], s[48:49]
	v_mov_b64_e32 v[16:17], s[50:51]
	v_max_f32_e32 v42, v19, v19
	v_max_f32_e32 v43, v18, v18
	v_max_f32_e32 v42, v43, v42
	v_max3_f32 v42, v42, v20, v21
	v_max3_f32 v42, v42, v22, v23
	v_max3_f32 v42, v42, v24, v25
	v_max3_f32 v42, v42, v26, v27
	v_max3_f32 v42, v42, v28, v29
	v_max3_f32 v50, v42, v30, v31
	v_mfma_f32_32x32x64_f8f6f4 v[34:49], v[34:41], v[154:161], 0
	v_max3_f32 v50, v50, v32, v33
	s_cmp_lg_u32 0, -1
	s_cselect_b32 s37, 0, 0
	v_mov_b32_e32 v130, v181
	v_mov_b32_e32 v131, v181
	s_add_i32 s38, s37, 0x1000
	s_waitcnt vmcnt(0) lgkmcnt(0)
	s_barrier
	v_add_u32_e32 v207, s38, v194
	v_add_u32_e32 v209, v207, v195
	s_nop 11
	v_max3_f32 v50, v50, v34, v35
	v_max3_f32 v50, v50, v36, v37
	v_max3_f32 v50, v50, v38, v39
	v_max3_f32 v50, v50, v40, v41
	v_max3_f32 v50, v50, v42, v43
	v_max3_f32 v50, v50, v44, v45
	v_max3_f32 v50, v50, v46, v47
	v_max3_f32 v50, v50, v48, v49
	v_mov_b32_e32 v51, v50
	s_nop 1
	v_permlane32_swap_b32_e32 v50, v51
	v_max_f32_e32 v51, v51, v51
	v_max_f32_e32 v50, v50, v50
	v_max_f32_e32 v50, v50, v51
	s_cmp_eq_u32 s98, 0
	s_cselect_b32 s100, 0x40000000, 0xc0600000
	v_add_f32_e32 v198, s100, v50
	v_sub_f32_e32 v18, v18, v198
	v_sub_f32_e32 v19, v19, v198
	v_sub_f32_e32 v22, v22, v198
	v_sub_f32_e32 v23, v23, v198
	v_exp_f32_e32 v50, v18
	v_exp_f32_e32 v51, v19
	v_exp_f32_e32 v54, v22
	v_exp_f32_e32 v55, v23
	v_xor_b32_e32 v82, 0x80000000, v198
	v_sub_f32_e32 v20, v20, v198
	v_sub_f32_e32 v21, v21, v198
	v_sub_f32_e32 v24, v24, v198
	v_sub_f32_e32 v25, v25, v198
	v_mov_b32_e32 v83, v82
	v_mov_b32_e32 v84, v82
	v_mov_b32_e32 v85, v82
	v_mov_b32_e32 v86, v82
	v_mov_b32_e32 v87, v82
	v_mov_b32_e32 v88, v82
	v_mov_b32_e32 v89, v82
	v_mov_b32_e32 v90, v82
	v_mov_b32_e32 v91, v82
	v_mov_b32_e32 v92, v82
	v_mov_b32_e32 v93, v82
	v_mov_b32_e32 v94, v82
	v_mov_b32_e32 v95, v82
	v_mov_b32_e32 v96, v82
	v_mov_b32_e32 v97, v82
	v_exp_f32_e32 v52, v20
	v_exp_f32_e32 v53, v21
	v_exp_f32_e32 v56, v24
	v_exp_f32_e32 v57, v25
	v_cvt_pk_fp8_f32 v130, v50, v51
	v_cvt_pk_fp8_f32 v131, v54, v55
	ds_read_b128 v[18:21], v207 offset:0
	v_sub_f32_e32 v26, v26, v198
	v_sub_f32_e32 v27, v27, v198
	v_sub_f32_e32 v28, v28, v198
	v_sub_f32_e32 v29, v29, v198
	ds_read_b128 v[22:25], v209 offset:0
	v_sub_f32_e32 v34, v34, v198
	v_sub_f32_e32 v35, v35, v198
	v_sub_f32_e32 v36, v36, v198
	v_sub_f32_e32 v37, v37, v198
	v_sub_f32_e32 v38, v38, v198
	v_sub_f32_e32 v39, v39, v198
	v_sub_f32_e32 v40, v40, v198
	v_sub_f32_e32 v41, v41, v198
	v_sub_f32_e32 v42, v42, v198
	v_sub_f32_e32 v43, v43, v198
	v_sub_f32_e32 v44, v44, v198
	v_sub_f32_e32 v45, v45, v198
	v_sub_f32_e32 v30, v30, v198
	v_sub_f32_e32 v46, v46, v198
	v_sub_f32_e32 v31, v31, v198
	v_sub_f32_e32 v47, v47, v198
	v_sub_f32_e32 v32, v32, v198
	v_sub_f32_e32 v48, v48, v198
	v_sub_f32_e32 v33, v33, v198
	v_sub_f32_e32 v49, v49, v198
	v_exp_f32_e32 v58, v26
	v_exp_f32_e32 v59, v27
	v_exp_f32_e32 v60, v28
	v_exp_f32_e32 v61, v29
	ds_read_b128 v[26:29], v207 offset:0x800
	v_exp_f32_e32 v34, v34
	v_exp_f32_e32 v35, v35
	v_exp_f32_e32 v36, v36
	v_exp_f32_e32 v37, v37
	v_exp_f32_e32 v38, v38
	v_exp_f32_e32 v39, v39
	v_exp_f32_e32 v40, v40
	v_exp_f32_e32 v41, v41
	v_exp_f32_e32 v42, v42
	v_exp_f32_e32 v43, v43
	v_exp_f32_e32 v44, v44
	v_exp_f32_e32 v45, v45
	v_exp_f32_e32 v62, v30
	v_exp_f32_e32 v46, v46
	v_exp_f32_e32 v63, v31
	v_exp_f32_e32 v47, v47
	v_exp_f32_e32 v64, v32
	v_exp_f32_e32 v48, v48
	v_exp_f32_e32 v65, v33
	v_exp_f32_e32 v49, v49
	ds_read_b128 v[30:33], v209 offset:0x800
	v_cvt_pk_fp8_f32 v130, v52, v53 op_sel:[0,0,1]
	v_cvt_pk_fp8_f32 v131, v56, v57 op_sel:[0,0,1]
	s_waitcnt lgkmcnt(2)
	v_mfma_f32_32x32x64_f8f6f4 v[98:113], v[18:25], v[154:161], v[82:97]
	v_mov_b32_e32 v132, v181
	v_mov_b32_e32 v133, v181
	v_cvt_pk_fp8_f32 v132, v58, v59
	v_cvt_pk_fp8_f32 v133, v62, v63
	ds_read_b128 v[170:173], v188 offset:0
	ds_read_b128 v[174:177], v189 offset:0
	v_cvt_pk_fp8_f32 v132, v60, v61 op_sel:[0,0,1]
	v_cvt_pk_fp8_f32 v133, v64, v65 op_sel:[0,0,1]
	s_waitcnt lgkmcnt(2)
	v_mov_b64_e32 v[128:129], v[96:97]
	v_mov_b64_e32 v[126:127], v[94:95]
	v_mov_b64_e32 v[124:125], v[92:93]
	v_mov_b64_e32 v[122:123], v[90:91]
	v_mov_b64_e32 v[120:121], v[88:89]
	v_mov_b64_e32 v[118:119], v[86:87]
	v_mov_b64_e32 v[116:117], v[84:85]
	v_mov_b64_e32 v[114:115], v[82:83]
	v_mov_b32_e32 v134, v181
	v_mov_b32_e32 v135, v181
	v_mfma_f32_32x32x64_f8f6f4 v[114:129], v[26:33], v[154:161], v[114:129]
	v_mov_b32_e32 v136, v181
	v_mov_b32_e32 v137, v181
	v_cvt_pk_fp8_f32 v134, v34, v35
	v_cvt_pk_fp8_f32 v135, v38, v39
	v_cvt_pk_fp8_f32 v136, v42, v43
	v_cvt_pk_fp8_f32 v137, v46, v47
	v_cvt_pk_fp8_f32 v134, v36, v37 op_sel:[0,0,1]
	v_cvt_pk_fp8_f32 v135, v40, v41 op_sel:[0,0,1]
	v_cvt_pk_fp8_f32 v136, v44, v45 op_sel:[0,0,1]
	v_cvt_pk_fp8_f32 v137, v48, v49 op_sel:[0,0,1]
	s_nop 0
	ds_read_b128 v[138:141], v188 offset:0x800
	ds_read_b128 v[142:145], v189 offset:0x800
	s_nop 0
	v_mfma_f32_16x16x128_f8f6f4 v[18:21], v[130:137], v[146:153], 0
	s_add_i32 s38, s37, 0x2000
	v_add_u32_e32 v205, s38, v194
	s_add_i32 s38, s37, 0x6000
	v_add_u32_e32 v203, s38, v194
	s_add_i32 s38, s37, 0x3000
	s_waitcnt vmcnt(0) lgkmcnt(0)
	s_barrier
	v_add_u32_e32 v201, s38, v194
	s_add_i32 s38, s37, 0x8000
	s_add_i32 s37, s37, 0xa000
	v_add_u32_e32 v199, s38, v194
	v_add_u32_e32 v196, s37, v194
	v_mov_b64_e32 v[48:49], v[16:17]
	v_mov_b64_e32 v[64:65], v[16:17]
	v_mov_b64_e32 v[80:81], v[16:17]
	v_add_u32_e32 v206, v205, v195
	v_add_u32_e32 v204, v203, v195
	v_add_u32_e32 v202, v201, v195
	v_add_u32_e32 v200, v199, v195
	v_add_u32_e32 v197, v196, v195
	s_mov_b32 s37, -2
	v_mov_b64_e32 v[46:47], v[14:15]
	v_mov_b64_e32 v[44:45], v[12:13]
	v_mov_b64_e32 v[42:43], v[10:11]
	v_mov_b64_e32 v[40:41], v[8:9]
	v_mov_b64_e32 v[38:39], v[6:7]
	v_mov_b64_e32 v[36:37], v[4:5]
	v_mov_b64_e32 v[34:35], v[2:3]
	v_mov_b64_e32 v[62:63], v[14:15]
	v_mov_b64_e32 v[60:61], v[12:13]
	v_mov_b64_e32 v[58:59], v[10:11]
	v_mov_b64_e32 v[56:57], v[8:9]
	v_mov_b64_e32 v[54:55], v[6:7]
	v_mov_b64_e32 v[52:53], v[4:5]
	v_mov_b64_e32 v[50:51], v[2:3]
	v_mov_b64_e32 v[78:79], v[14:15]
	v_mov_b64_e32 v[76:77], v[12:13]
	v_mov_b64_e32 v[74:75], v[10:11]
	v_mov_b64_e32 v[72:73], v[8:9]
	v_mov_b64_e32 v[70:71], v[6:7]
	v_mov_b64_e32 v[68:69], v[4:5]
	v_mov_b64_e32 v[66:67], v[2:3]
	s_branch .LBB0_1327

.LBB0_1376:
	s_and_b64 vcc, exec, s[38:39]
	s_cbranch_vccz .LBB0_1202
	ds_read_b128 v[18:21], v183 offset:0
	ds_read_b128 v[22:25], v190 offset:0
	ds_read_b128 v[34:37], v183 offset:0x800
	ds_read_b128 v[38:41], v190 offset:0x800
	s_waitcnt lgkmcnt(0)
	s_waitcnt vmcnt(0)
	s_nop 11
	v_mfma_f32_32x32x64_f8f6f4 v[18:33], v[18:25], v[154:161], 0
	s_mov_b32 s37, s36
	s_mov_b32 s38, s36
	s_mov_b32 s39, s36
	s_mov_b32 s40, s36
	s_mov_b32 s41, s36
	s_mov_b32 s42, s36
	s_mov_b32 s43, s36
	s_mov_b32 s44, s36
	s_mov_b32 s45, s36
	s_mov_b32 s46, s36
	s_mov_b32 s47, s36
	s_mov_b32 s48, s36
	s_mov_b32 s49, s36
	s_mov_b32 s50, s36
	s_mov_b32 s51, s36
	v_mov_b64_e32 v[2:3], s[36:37]
	v_mov_b64_e32 v[4:5], s[38:39]
	v_mov_b64_e32 v[6:7], s[40:41]
	v_mov_b64_e32 v[8:9], s[42:43]
	v_mov_b64_e32 v[10:11], s[44:45]
	v_mov_b64_e32 v[12:13], s[46:47]
	v_mov_b64_e32 v[14:15], s[48:49]
	v_mov_b64_e32 v[16:17], s[50:51]
	v_max_f32_e32 v42, v19, v19
	v_max_f32_e32 v43, v18, v18
	v_max_f32_e32 v42, v43, v42
	v_max3_f32 v42, v42, v20, v21
	v_max3_f32 v42, v42, v22, v23
	v_max3_f32 v42, v42, v24, v25
	v_max3_f32 v42, v42, v26, v27
	v_max3_f32 v42, v42, v28, v29
	v_max3_f32 v50, v42, v30, v31
	v_mfma_f32_32x32x64_f8f6f4 v[34:49], v[34:41], v[154:161], 0
	v_max3_f32 v50, v50, v32, v33
	s_lshl_b32 s45, s95, 10
	s_lshl_b32 s46, s81, 10
	s_cmp_lg_u32 0, -1
	s_cselect_b32 s38, 0, 0
	s_add_i32 s37, s38, 0x2000
	s_add_i32 s39, s38, 0x3000
	s_add_i32 s6, s38, 0x1000
	v_add_u32_e32 v203, s37, v194
	s_add_i32 s37, s38, 0x6000
	v_add_u32_e32 v199, s39, v194
	s_add_i32 s39, s38, 0x8000
	s_add_i32 s38, s38, 0xa000
	v_add_u32_e32 v205, s6, v194
	v_add_u32_e32 v201, s37, v194
	s_nop 4
	v_max3_f32 v50, v50, v34, v35
	v_max3_f32 v50, v50, v36, v37
	v_max3_f32 v50, v50, v38, v39
	v_max3_f32 v50, v50, v40, v41
	v_max3_f32 v50, v50, v42, v43
	v_max3_f32 v50, v50, v44, v45
	v_max3_f32 v50, v50, v46, v47
	v_max3_f32 v50, v50, v48, v49
	v_mov_b32_e32 v51, v50
	s_nop 1
	v_permlane32_swap_b32_e32 v50, v51
	v_max_f32_e32 v51, v51, v51
	v_max_f32_e32 v50, v50, v50
	v_max_f32_e32 v50, v50, v51
	s_cmp_eq_u32 s98, 0
	s_cselect_b32 s100, 0x40000000, 0xc0600000
	v_add_f32_e32 v198, s100, v50
	v_sub_f32_e32 v18, v18, v198
	v_sub_f32_e32 v19, v19, v198
	v_add_u32_e32 v196, s39, v194
	v_add_u32_e32 v194, s38, v194
	s_lshl_b32 s38, s80, 4
	v_exp_f32_e32 v114, v18
	v_exp_f32_e32 v115, v19
	v_lshl_add_u64 v[18:19], s[16:17], 0, v[180:181]
	s_and_b32 s38, s38, 0xfffffc00
	s_ashr_i32 s89, s88, 31
	s_or_b32 s40, s88, 0x100
	s_add_i32 s41, s94, 0x4100
	s_or_b32 s42, s88, 0x140
	s_add_i32 s43, s94, 0x4140
	v_lshl_add_u64 v[170:171], v[18:19], 0, s[28:29]
	v_lshl_or_b32 v18, v193, 4, s38
	s_lshl_b64 s[38:39], s[88:89], 10
	s_add_u32 s38, s38, s87
	v_xor_b32_e32 v82, 0x80000000, v198
	v_sub_f32_e32 v34, v34, v198
	v_sub_f32_e32 v35, v35, v198
	v_sub_f32_e32 v20, v20, v198
	v_sub_f32_e32 v36, v36, v198
	v_sub_f32_e32 v21, v21, v198
	v_sub_f32_e32 v37, v37, v198
	v_sub_f32_e32 v22, v22, v198
	v_sub_f32_e32 v38, v38, v198
	v_sub_f32_e32 v23, v23, v198
	v_sub_f32_e32 v39, v39, v198
	v_sub_f32_e32 v24, v24, v198
	v_sub_f32_e32 v40, v40, v198
	v_sub_f32_e32 v25, v25, v198
	v_sub_f32_e32 v41, v41, v198
	v_sub_f32_e32 v26, v26, v198
	v_sub_f32_e32 v42, v42, v198
	v_sub_f32_e32 v27, v27, v198
	v_sub_f32_e32 v43, v43, v198
	v_sub_f32_e32 v28, v28, v198
	v_sub_f32_e32 v44, v44, v198
	v_sub_f32_e32 v29, v29, v198
	v_sub_f32_e32 v45, v45, v198
	v_sub_f32_e32 v30, v30, v198
	v_sub_f32_e32 v46, v46, v198
	v_sub_f32_e32 v31, v31, v198
	v_sub_f32_e32 v47, v47, v198
	v_sub_f32_e32 v32, v32, v198
	v_sub_f32_e32 v48, v48, v198
	v_sub_f32_e32 v33, v33, v198
	v_sub_f32_e32 v49, v49, v198
	s_addc_u32 s39, s39, s76
	v_mov_b32_e32 v83, v82
	v_mov_b32_e32 v84, v82
	v_mov_b32_e32 v85, v82
	v_mov_b32_e32 v86, v82
	v_mov_b32_e32 v87, v82
	v_mov_b32_e32 v88, v82
	v_mov_b32_e32 v89, v82
	v_mov_b32_e32 v90, v82
	v_mov_b32_e32 v91, v82
	v_mov_b32_e32 v92, v82
	v_mov_b32_e32 v93, v82
	v_mov_b32_e32 v94, v82
	v_mov_b32_e32 v95, v82
	v_mov_b32_e32 v96, v82
	v_mov_b32_e32 v97, v82
	v_exp_f32_e32 v98, v34
	v_exp_f32_e32 v99, v35
	v_exp_f32_e32 v116, v20
	v_exp_f32_e32 v100, v36
	v_exp_f32_e32 v117, v21
	v_exp_f32_e32 v101, v37
	v_exp_f32_e32 v118, v22
	v_exp_f32_e32 v102, v38
	v_exp_f32_e32 v119, v23
	v_exp_f32_e32 v103, v39
	v_exp_f32_e32 v120, v24
	v_exp_f32_e32 v104, v40
	v_exp_f32_e32 v121, v25
	v_exp_f32_e32 v105, v41
	v_exp_f32_e32 v122, v26
	v_exp_f32_e32 v106, v42
	v_exp_f32_e32 v123, v27
	v_exp_f32_e32 v107, v43
	v_exp_f32_e32 v124, v28
	v_exp_f32_e32 v108, v44
	v_exp_f32_e32 v125, v29
	v_exp_f32_e32 v109, v45
	v_exp_f32_e32 v126, v30
	v_exp_f32_e32 v110, v46
	v_exp_f32_e32 v127, v31
	v_exp_f32_e32 v111, v47
	v_exp_f32_e32 v128, v32
	v_exp_f32_e32 v112, v48
	v_exp_f32_e32 v129, v33
	v_exp_f32_e32 v113, v49
	v_mov_b32_e32 v19, v181
	s_add_u32 s38, s38, 0x29c30040
	s_waitcnt vmcnt(3) lgkmcnt(0)
	s_barrier
	v_lshl_add_u64 v[172:173], s[92:93], 0, v[18:19]
	s_addc_u32 s39, s39, 0
	v_add3_u32 v18, s79, v191, v192
	v_lshl_add_u64 v[174:175], s[38:39], 0, v[18:19]
	v_mov_b32_e32 v162, 0
	v_mov_b64_e32 v[48:49], v[16:17]
	v_mov_b64_e32 v[64:65], v[16:17]
	v_mov_b64_e32 v[80:81], v[16:17]
	v_mov_b64_e32 v[32:33], v[16:17]
	v_add_u32_e32 v206, v205, v195
	v_cmp_gt_u32_e64 s[6:7], 32, v193
	v_add_u32_e32 v204, v203, v195
	v_add_u32_e32 v202, v201, v195
	s_movk_i32 s37, 0x100
	v_add_u32_e32 v200, v199, v195
	v_add_u32_e32 v197, v196, v195
	v_add_u32_e32 v195, v194, v195
	s_mov_b32 s44, -3
	s_add_i32 s45, s45, 0
	s_add_i32 s46, s46, 0
	v_mov_b64_e32 v[46:47], v[14:15]
	v_mov_b64_e32 v[44:45], v[12:13]
	v_mov_b64_e32 v[42:43], v[10:11]
	v_mov_b64_e32 v[40:41], v[8:9]
	v_mov_b64_e32 v[38:39], v[6:7]
	v_mov_b64_e32 v[36:37], v[4:5]
	v_mov_b64_e32 v[34:35], v[2:3]
	v_mov_b64_e32 v[62:63], v[14:15]
	v_mov_b64_e32 v[60:61], v[12:13]
	v_mov_b64_e32 v[58:59], v[10:11]
	v_mov_b64_e32 v[56:57], v[8:9]
	v_mov_b64_e32 v[54:55], v[6:7]
	v_mov_b64_e32 v[52:53], v[4:5]
	v_mov_b64_e32 v[50:51], v[2:3]
	v_mov_b64_e32 v[78:79], v[14:15]
	v_mov_b64_e32 v[76:77], v[12:13]
	v_mov_b64_e32 v[74:75], v[10:11]
	v_mov_b64_e32 v[72:73], v[8:9]
	v_mov_b64_e32 v[70:71], v[6:7]
	v_mov_b64_e32 v[68:69], v[4:5]
	v_mov_b64_e32 v[66:67], v[2:3]
	v_mov_b64_e32 v[30:31], v[14:15]
	v_mov_b64_e32 v[28:29], v[12:13]
	v_mov_b64_e32 v[26:27], v[10:11]
	v_mov_b64_e32 v[24:25], v[8:9]
	v_mov_b64_e32 v[22:23], v[6:7]
	v_mov_b64_e32 v[20:21], v[4:5]
	v_mov_b64_e32 v[18:19], v[2:3]
	v_mov_b32_e32 v163, v162
	v_mov_b32_e32 v164, v162
	v_mov_b32_e32 v165, v162
	v_mov_b32_e32 v166, v162
	v_mov_b32_e32 v167, v162
	v_mov_b32_e32 v168, v162
	v_mov_b32_e32 v169, v162
	s_branch .LBB0_1380
